# baseline (speedup 1.0000x reference)
.Lk_15:
	global_load_dword v66, v[62:63], off offset:4
	global_load_dword v67, v[62:63], off offset:260
	global_load_dword v68, v[62:63], off offset:516
	global_load_dword v69, v[62:63], off offset:772
	global_load_dword v70, v[64:65], off offset:4
	global_load_dword v71, v[64:65], off offset:260
	global_load_dword v72, v[64:65], off offset:516
	global_load_dword v73, v[64:65], off offset:772
	v_and_b32_e32 v62, 15, v0
	s_mov_b32 s8, 0x4038aa3b
	s_waitcnt vmcnt(11)
	v_pk_mul_f32 v[38:39], v[50:51], v[38:39]
	v_lshlrev_b32_e32 v57, 2, v1
	s_lshl_b32 s10, s34, 8
	v_lshlrev_b32_e32 v1, 4, v62
	v_pk_add_f32 v[52:53], v[52:53], v[54:55]
	v_pk_add_f32 v[54:55], v[58:59], v[60:61]
	s_mov_b32 s9, 0xbfb8aa3b
	s_waitcnt vmcnt(10)
	v_pk_mul_f32 v[46:47], v[50:51], v[46:47]
	v_pk_mul_f32 v[48:49], v[50:51], v[48:49]
	v_pk_mul_f32 v[40:41], v[50:51], v[40:41]
	s_waitcnt vmcnt(8)
	v_pk_mul_f32 v[42:43], v[50:51], v[42:43]
	v_pk_mul_f32 v[44:45], v[50:51], v[44:45]
	v_pk_mul_f32 v[34:35], v[50:51], v[34:35]
	v_pk_mul_f32 v[36:37], v[50:51], v[36:37]
	v_pk_mul_f32 v[30:31], v[50:51], v[30:31]
	v_pk_mul_f32 v[32:33], v[50:51], v[32:33]
	v_pk_mul_f32 v[18:19], v[50:51], v[18:19]
	v_pk_mul_f32 v[58:59], v[50:51], v[20:21]
	v_pk_mul_f32 v[60:61], v[50:51], v[26:27]
	v_pk_mul_f32 v[64:65], v[50:51], v[28:29]
	v_pk_mul_f32 v[74:75], v[50:51], v[22:23]
	v_pk_mul_f32 v[50:51], v[50:51], v[24:25]
	v_cvt_pk_f16_f32 v24, v38, v39
	v_or3_b32 v38, v1, v57, s10
	v_lshlrev_b32_e32 v82, 4, v80
	s_and_b64 vcc, exec, s[6:7]
	s_mov_b32 s6, s9
	v_cvt_pk_f16_f32 v25, v40, v41
	v_add_u32_e32 v81, 0x23280, v38
	s_mov_b64 s[4:5], -1
	v_pk_mul_f32 v[20:21], v[54:55], s[8:9]
	v_cvt_pk_f16_f32 v22, v46, v47
	v_cvt_pk_f16_f32 v23, v48, v49
	v_cvt_pk_f16_f32 v26, v42, v43
	v_cvt_pk_f16_f32 v27, v44, v45
	v_cvt_pk_f16_f32 v28, v34, v35
	v_cvt_pk_f16_f32 v29, v36, v37
	v_cvt_pk_f16_f32 v30, v30, v31
	v_cvt_pk_f16_f32 v31, v32, v33
	v_cvt_pk_f16_f32 v32, v18, v19
	v_cvt_pk_f16_f32 v33, v58, v59
	v_cvt_pk_f16_f32 v34, v60, v61
	v_cvt_pk_f16_f32 v35, v64, v65
	v_cvt_pk_f16_f32 v36, v74, v75
	v_cvt_pk_f16_f32 v37, v50, v51
	v_add_u32_e32 v75, 0x23280, v82
	v_pk_mul_f32 v[18:19], v[52:53], s[6:7] op_sel_hi:[1,0]
	s_waitcnt lgkmcnt(0)
	s_barrier
	s_waitcnt vmcnt(2)
	v_pk_add_f32 v[38:39], v[66:67], v[70:71]
	s_nop 0
	v_pk_mul_f32 v[38:39], v[38:39], s[6:7] op_sel_hi:[1,0]
	s_waitcnt vmcnt(0)
	v_pk_add_f32 v[40:41], v[68:69], v[72:73]
	s_nop 0
	v_pk_mul_f32 v[40:41], v[40:41], s[8:9]
	s_cbranch_vccz .Lk_134
	s_setprio 0
	v_lshrrev_b32_e32 v42, 4, v80
	v_lshlrev_b32_e32 v42, 5, v42
	global_load_dwordx4 v[44:47], v42, s[18:19]
	global_load_dwordx4 v[48:51], v42, s[18:19] offset:16
	global_load_dwordx4 v[52:55], v42, s[18:19] offset:128
	global_load_dwordx4 v[56:59], v42, s[18:19] offset:144
	s_load_dword s28, s[20:21], 0x0
	v_and_b32_e32 v43, 15, v80
	v_cmp_eq_u32_e32 vcc, 1, v43
	v_cmp_eq_u32_e64 s[4:5], 0, v43
	v_cmp_gt_u32_e64 s[30:31], 16, v80
	v_lshl_or_b32 v124, s3, 4, v43
	v_mul_u32_u24_e32 v124, 0x708, v124
	v_lshlrev_b32_e32 v74, 2, v43
	v_add_u32_e32 v74, 0x1c200, v74
	v_mov_b32_e32 v72, 0x3fe10966
	v_mov_b32_e32 v73, 0xbfe10966
	v_mov_b32_e32 v92, 0xc038aa3b
	v_mov_b32_e32 v93, 0xc038aa3b
	s_mov_b32 s8, 0x4038aa3b
	s_mov_b32 s9, 0
	v_mov_b32_e32 v64, 0
	v_mov_b32_e32 v65, 0
	s_mov_b32 s12, 4
	s_waitcnt vmcnt(0) lgkmcnt(0)
	v_cvt_f16_f32_e32 v60, v44
	v_cvt_f32_f16_e32 v61, v60
	v_sub_f32_e32 v61, v44, v61
	v_cvt_f16_f32_e32 v61, v61
	v_cndmask_b32_e32 v61, 0, v61, vcc
	v_cndmask_b32_e64 v94, v61, v60, s[4:5]
	v_cvt_f16_f32_e32 v60, v45
	v_cvt_f32_f16_e32 v61, v60
	v_sub_f32_e32 v61, v45, v61
	v_cvt_f16_f32_e32 v61, v61
	v_cndmask_b32_e32 v61, 0, v61, vcc
	v_cndmask_b32_e64 v95, v61, v60, s[4:5]
	v_cvt_f16_f32_e32 v60, v46
	v_cvt_f32_f16_e32 v61, v60
	v_sub_f32_e32 v61, v46, v61
	v_cvt_f16_f32_e32 v61, v61
	v_cndmask_b32_e32 v61, 0, v61, vcc
	v_cndmask_b32_e64 v96, v61, v60, s[4:5]
	v_cvt_f16_f32_e32 v60, v47
	v_cvt_f32_f16_e32 v61, v60
	v_sub_f32_e32 v61, v47, v61
	v_cvt_f16_f32_e32 v61, v61
	v_cndmask_b32_e32 v61, 0, v61, vcc
	v_cndmask_b32_e64 v97, v61, v60, s[4:5]
	v_cvt_f16_f32_e32 v60, v48
	v_cvt_f32_f16_e32 v61, v60
	v_sub_f32_e32 v61, v48, v61
	v_cvt_f16_f32_e32 v61, v61
	v_cndmask_b32_e32 v61, 0, v61, vcc
	v_cndmask_b32_e64 v98, v61, v60, s[4:5]
	v_cvt_f16_f32_e32 v60, v49
	v_cvt_f32_f16_e32 v61, v60
	v_sub_f32_e32 v61, v49, v61
	v_cvt_f16_f32_e32 v61, v61
	v_cndmask_b32_e32 v61, 0, v61, vcc
	v_cndmask_b32_e64 v99, v61, v60, s[4:5]
	v_cvt_f16_f32_e32 v60, v50
	v_cvt_f32_f16_e32 v61, v60
	v_sub_f32_e32 v61, v50, v61
	v_cvt_f16_f32_e32 v61, v61
	v_cndmask_b32_e32 v61, 0, v61, vcc
	v_cndmask_b32_e64 v100, v61, v60, s[4:5]
	v_cvt_f16_f32_e32 v60, v51
	v_cvt_f32_f16_e32 v61, v60
	v_sub_f32_e32 v61, v51, v61
	v_cvt_f16_f32_e32 v61, v61
	v_cndmask_b32_e32 v61, 0, v61, vcc
	v_cndmask_b32_e64 v101, v61, v60, s[4:5]
	v_cvt_f16_f32_e32 v60, v52
	v_cvt_f32_f16_e32 v61, v60
	v_sub_f32_e32 v61, v52, v61
	v_cvt_f16_f32_e32 v61, v61
	v_cndmask_b32_e32 v61, 0, v61, vcc
	v_cndmask_b32_e64 v102, v61, v60, s[4:5]
	v_cvt_f16_f32_e32 v60, v53
	v_cvt_f32_f16_e32 v61, v60
	v_sub_f32_e32 v61, v53, v61
	v_cvt_f16_f32_e32 v61, v61
	v_cndmask_b32_e32 v61, 0, v61, vcc
	v_cndmask_b32_e64 v103, v61, v60, s[4:5]
	v_cvt_f16_f32_e32 v60, v54
	v_cvt_f32_f16_e32 v61, v60
	v_sub_f32_e32 v61, v54, v61
	v_cvt_f16_f32_e32 v61, v61
	v_cndmask_b32_e32 v61, 0, v61, vcc
	v_cndmask_b32_e64 v104, v61, v60, s[4:5]
	v_cvt_f16_f32_e32 v60, v55
	v_cvt_f32_f16_e32 v61, v60
	v_sub_f32_e32 v61, v55, v61
	v_cvt_f16_f32_e32 v61, v61
	v_cndmask_b32_e32 v61, 0, v61, vcc
	v_cndmask_b32_e64 v105, v61, v60, s[4:5]
	v_cvt_f16_f32_e32 v60, v56
	v_cvt_f32_f16_e32 v61, v60
	v_sub_f32_e32 v61, v56, v61
	v_cvt_f16_f32_e32 v61, v61
	v_cndmask_b32_e32 v61, 0, v61, vcc
	v_cndmask_b32_e64 v106, v61, v60, s[4:5]
	v_cvt_f16_f32_e32 v60, v57
	v_cvt_f32_f16_e32 v61, v60
	v_sub_f32_e32 v61, v57, v61
	v_cvt_f16_f32_e32 v61, v61
	v_cndmask_b32_e32 v61, 0, v61, vcc
	v_cndmask_b32_e64 v107, v61, v60, s[4:5]
	v_cvt_f16_f32_e32 v60, v58
	v_cvt_f32_f16_e32 v61, v60
	v_sub_f32_e32 v61, v58, v61
	v_cvt_f16_f32_e32 v61, v61
	v_cndmask_b32_e32 v61, 0, v61, vcc
	v_cndmask_b32_e64 v108, v61, v60, s[4:5]
	v_cvt_f16_f32_e32 v60, v59
	v_cvt_f32_f16_e32 v61, v60
	v_sub_f32_e32 v61, v59, v61
	v_cvt_f16_f32_e32 v61, v61
	v_cndmask_b32_e32 v61, 0, v61, vcc
	v_cndmask_b32_e64 v109, v61, v60, s[4:5]
	v_pack_b32_f16 v116, v94, v95
	v_pack_b32_f16 v117, v96, v97
	v_pack_b32_f16 v118, v98, v99
	v_pack_b32_f16 v119, v100, v101
	v_pack_b32_f16 v120, v102, v103
	v_pack_b32_f16 v121, v104, v105
	v_pack_b32_f16 v122, v106, v107
	v_pack_b32_f16 v123, v108, v109
	s_cmp_eq_u32 s34, 0
	s_cbranch_scc1 .Lcb_r0
	s_cmp_eq_u32 s34, 1
	s_cbranch_scc1 .Lcb_r1
	s_cmp_eq_u32 s34, 2
	s_cbranch_scc1 .Lcb_r2
	s_barrier
	ds_read_b128 v[44:47], v75 offset:0
	ds_read_b128 v[68:71], v75 offset:1024
	s_waitcnt lgkmcnt(0)
	v_mfma_f32_16x16x32_f16 v[84:87], v[2:5], v[44:47], v[18:21]
	v_mfma_f32_16x16x32_f16 v[88:91], v[14:17], v[44:47], v[38:41]
	v_mfma_f32_16x16x32_f16 v[84:87], v[6:9], v[68:71], v[84:87]
	v_mfma_f32_16x16x32_f16 v[88:91], v[10:13], v[68:71], v[88:91]
	s_barrier
	ds_read_b128 v[56:59], v75 offset:6144
	ds_read_b128 v[60:63], v75 offset:7168
	s_waitcnt lgkmcnt(1)
	v_mfma_f32_16x16x32_f16 v[84:87], v[30:33], v[56:59], v[84:87]
	v_mfma_f32_16x16x32_f16 v[88:91], v[22:25], v[56:59], v[88:91]
	s_waitcnt lgkmcnt(0)
	v_mfma_f32_16x16x32_f16 v[84:87], v[34:37], v[60:63], v[84:87]
	v_mfma_f32_16x16x32_f16 v[88:91], v[26:29], v[60:63], v[88:91]
	ds_read_b128 v[44:47], v75 offset:2048
	ds_read_b128 v[68:71], v75 offset:3072
	s_nop 7
	v_exp_f32_e32 v94, v86
	v_exp_f32_e32 v95, v90
	v_exp_f32_e32 v96, v84
	v_exp_f32_e32 v97, v88
	v_exp_f32_e32 v98, v85
	v_exp_f32_e32 v99, v89
	v_pk_add_f32 v[100:101], v[94:95], 1.0 op_sel_hi:[1,0]
	v_pk_fma_f32 v[102:103], v[94:95], s[8:9], v[92:93] op_sel_hi:[1,0,0]
	v_pk_fma_f32 v[100:101], v[96:97], v[100:101], v[100:101]
	v_pk_fma_f32 v[104:105], v[100:101], v[98:99], v[100:101]
	v_rcp_f32_e32 v104, v104
	v_rcp_f32_e32 v105, v105
	v_pk_fma_f32 v[102:103], v[102:103], v[98:99], v[102:103]
	v_pk_fma_f32 v[102:103], v[64:65], v[100:101], v[102:103]
	v_exp_f32_e32 v106, v87
	v_pk_mul_f32 v[64:65], v[102:103], v[104:105]
	v_exp_f32_e32 v108, v64
	v_exp_f32_e32 v109, v65
	v_exp_f32_e32 v107, v91
	v_pk_add_f32 v[110:111], v[108:109], 1.0 op_sel_hi:[1,0]
	v_pk_fma_f32 v[110:111], v[110:111], v[106:107], v[110:111]
	v_rcp_f32_e32 v110, v110
	v_rcp_f32_e32 v111, v111
	v_pk_add_f32 v[112:113], v[108:109], -1.0 op_sel_hi:[1,0]
	v_pk_mul_f32 v[112:113], v[112:113], v[110:111]
	v_cvt_pk_f16_f32 v114, v112, v113
	ds_write_b32 v81, v114 offset:4096
	s_waitcnt lgkmcnt(1)
	v_mfma_f32_16x16x32_f16 v[84:87], v[2:5], v[44:47], v[18:21]
	v_mfma_f32_16x16x32_f16 v[88:91], v[14:17], v[44:47], v[38:41]
	v_mfma_f32_16x16x32_f16 v[84:87], v[6:9], v[68:71], v[84:87]
	v_mfma_f32_16x16x32_f16 v[88:91], v[10:13], v[68:71], v[88:91]
	s_waitcnt lgkmcnt(0)
	s_barrier
	ds_read_b128 v[56:59], v75 offset:4096
	ds_read_b128 v[60:63], v75 offset:5120
	s_waitcnt lgkmcnt(1)
	v_mfma_f32_16x16x32_f16 v[84:87], v[30:33], v[56:59], v[84:87]
	v_mfma_f32_16x16x32_f16 v[88:91], v[22:25], v[56:59], v[88:91]
	s_waitcnt lgkmcnt(0)
	v_mfma_f32_16x16x32_f16 v[84:87], v[34:37], v[60:63], v[84:87]
	v_mfma_f32_16x16x32_f16 v[88:91], v[26:29], v[60:63], v[88:91]
	ds_read_b128 v[44:47], v75 offset:0
	ds_read_b128 v[68:71], v75 offset:1024
	s_nop 7
	v_exp_f32_e32 v94, v86
	v_exp_f32_e32 v95, v90
	v_exp_f32_e32 v96, v84
	v_exp_f32_e32 v97, v88
	v_exp_f32_e32 v98, v85
	v_exp_f32_e32 v99, v89
	v_pk_add_f32 v[100:101], v[94:95], 1.0 op_sel_hi:[1,0]
	v_pk_fma_f32 v[102:103], v[94:95], s[8:9], v[92:93] op_sel_hi:[1,0,0]
	v_pk_fma_f32 v[100:101], v[96:97], v[100:101], v[100:101]
	v_pk_fma_f32 v[104:105], v[100:101], v[98:99], v[100:101]
	v_rcp_f32_e32 v104, v104
	v_rcp_f32_e32 v105, v105
	v_pk_fma_f32 v[102:103], v[102:103], v[98:99], v[102:103]
	v_pk_fma_f32 v[102:103], v[64:65], v[100:101], v[102:103]
	v_exp_f32_e32 v106, v87
	v_pk_mul_f32 v[64:65], v[102:103], v[104:105]
	v_exp_f32_e32 v108, v64
	v_exp_f32_e32 v109, v65
	v_exp_f32_e32 v107, v91
	v_pk_add_f32 v[110:111], v[108:109], 1.0 op_sel_hi:[1,0]
	v_pk_fma_f32 v[110:111], v[110:111], v[106:107], v[110:111]
	v_rcp_f32_e32 v110, v110
	v_rcp_f32_e32 v111, v111
	v_pk_add_f32 v[112:113], v[108:109], -1.0 op_sel_hi:[1,0]
	v_pk_mul_f32 v[112:113], v[112:113], v[110:111]
	v_cvt_pk_f16_f32 v114, v112, v113
	ds_write_b32 v81, v114 offset:6144
	s_waitcnt lgkmcnt(1)
	v_mfma_f32_16x16x32_f16 v[84:87], v[2:5], v[44:47], v[18:21]
	v_mfma_f32_16x16x32_f16 v[88:91], v[14:17], v[44:47], v[38:41]
	v_mfma_f32_16x16x32_f16 v[84:87], v[6:9], v[68:71], v[84:87]
	v_mfma_f32_16x16x32_f16 v[88:91], v[10:13], v[68:71], v[88:91]
	s_waitcnt lgkmcnt(0)
	.p2align	6
.Lcb3_loop:
	s_barrier
	ds_read_b128 v[56:59], v75 offset:6144
	ds_read_b128 v[60:63], v75 offset:7168
	s_waitcnt lgkmcnt(1)
	v_mfma_f32_16x16x32_f16 v[84:87], v[30:33], v[56:59], v[84:87]
	v_mfma_f32_16x16x32_f16 v[88:91], v[22:25], v[56:59], v[88:91]
	s_waitcnt lgkmcnt(0)
	v_mfma_f32_16x16x32_f16 v[84:87], v[34:37], v[60:63], v[84:87]
	v_mfma_f32_16x16x32_f16 v[88:91], v[26:29], v[60:63], v[88:91]
	ds_read_b128 v[44:47], v75 offset:2048
	ds_read_b128 v[68:71], v75 offset:3072
	s_nop 7
	v_exp_f32_e32 v94, v86
	v_exp_f32_e32 v95, v90
	v_exp_f32_e32 v96, v84
	v_exp_f32_e32 v97, v88
	v_exp_f32_e32 v98, v85
	v_exp_f32_e32 v99, v89
	v_pk_add_f32 v[100:101], v[94:95], 1.0 op_sel_hi:[1,0]
	v_pk_fma_f32 v[102:103], v[94:95], s[8:9], v[92:93] op_sel_hi:[1,0,0]
	v_pk_fma_f32 v[100:101], v[96:97], v[100:101], v[100:101]
	v_pk_fma_f32 v[104:105], v[100:101], v[98:99], v[100:101]
	v_rcp_f32_e32 v104, v104
	v_rcp_f32_e32 v105, v105
	v_pk_fma_f32 v[102:103], v[102:103], v[98:99], v[102:103]
	v_pk_fma_f32 v[102:103], v[64:65], v[100:101], v[102:103]
	v_exp_f32_e32 v106, v87
	v_pk_mul_f32 v[64:65], v[102:103], v[104:105]
	v_exp_f32_e32 v108, v64
	v_exp_f32_e32 v109, v65
	v_exp_f32_e32 v107, v91
	v_pk_add_f32 v[110:111], v[108:109], 1.0 op_sel_hi:[1,0]
	v_pk_fma_f32 v[110:111], v[110:111], v[106:107], v[110:111]
	v_rcp_f32_e32 v110, v110
	v_rcp_f32_e32 v111, v111
	v_pk_add_f32 v[112:113], v[108:109], -1.0 op_sel_hi:[1,0]
	v_pk_mul_f32 v[112:113], v[112:113], v[110:111]
	v_cvt_pk_f16_f32 v114, v112, v113
	ds_write_b32 v81, v114 offset:4096
	s_waitcnt lgkmcnt(1)
	v_mfma_f32_16x16x32_f16 v[84:87], v[2:5], v[44:47], v[18:21]
	v_mfma_f32_16x16x32_f16 v[88:91], v[14:17], v[44:47], v[38:41]
	v_mfma_f32_16x16x32_f16 v[84:87], v[6:9], v[68:71], v[84:87]
	v_mfma_f32_16x16x32_f16 v[88:91], v[10:13], v[68:71], v[88:91]
	s_waitcnt lgkmcnt(0)
	s_barrier
	ds_read_b128 v[56:59], v75 offset:4096
	ds_read_b128 v[60:63], v75 offset:5120
	s_waitcnt lgkmcnt(1)
	v_mfma_f32_16x16x32_f16 v[84:87], v[30:33], v[56:59], v[84:87]
	v_mfma_f32_16x16x32_f16 v[88:91], v[22:25], v[56:59], v[88:91]
	s_waitcnt lgkmcnt(0)
	v_mfma_f32_16x16x32_f16 v[84:87], v[34:37], v[60:63], v[84:87]
	v_mfma_f32_16x16x32_f16 v[88:91], v[26:29], v[60:63], v[88:91]
	ds_read_b128 v[44:47], v75 offset:0
	ds_read_b128 v[68:71], v75 offset:1024
	s_nop 7
	v_exp_f32_e32 v94, v86
	v_exp_f32_e32 v95, v90
	v_exp_f32_e32 v96, v84
	v_exp_f32_e32 v97, v88
	v_exp_f32_e32 v98, v85
	v_exp_f32_e32 v99, v89
	v_pk_add_f32 v[100:101], v[94:95], 1.0 op_sel_hi:[1,0]
	v_pk_fma_f32 v[102:103], v[94:95], s[8:9], v[92:93] op_sel_hi:[1,0,0]
	v_pk_fma_f32 v[100:101], v[96:97], v[100:101], v[100:101]
	v_pk_fma_f32 v[104:105], v[100:101], v[98:99], v[100:101]
	v_rcp_f32_e32 v104, v104
	v_rcp_f32_e32 v105, v105
	v_pk_fma_f32 v[102:103], v[102:103], v[98:99], v[102:103]
	v_pk_fma_f32 v[102:103], v[64:65], v[100:101], v[102:103]
	v_exp_f32_e32 v106, v87
	v_pk_mul_f32 v[64:65], v[102:103], v[104:105]
	v_exp_f32_e32 v108, v64
	v_exp_f32_e32 v109, v65
	v_exp_f32_e32 v107, v91
	v_pk_add_f32 v[110:111], v[108:109], 1.0 op_sel_hi:[1,0]
	v_pk_fma_f32 v[110:111], v[110:111], v[106:107], v[110:111]
	v_rcp_f32_e32 v110, v110
	v_rcp_f32_e32 v111, v111
	v_pk_add_f32 v[112:113], v[108:109], -1.0 op_sel_hi:[1,0]
	v_pk_mul_f32 v[112:113], v[112:113], v[110:111]
	v_cvt_pk_f16_f32 v114, v112, v113
	ds_write_b32 v81, v114 offset:6144
	s_waitcnt lgkmcnt(1)
	v_mfma_f32_16x16x32_f16 v[84:87], v[2:5], v[44:47], v[18:21]
	v_mfma_f32_16x16x32_f16 v[88:91], v[14:17], v[44:47], v[38:41]
	v_mfma_f32_16x16x32_f16 v[84:87], v[6:9], v[68:71], v[84:87]
	v_mfma_f32_16x16x32_f16 v[88:91], v[10:13], v[68:71], v[88:91]
	s_waitcnt lgkmcnt(0)
	s_barrier
	ds_read_b128 v[56:59], v75 offset:6144
	ds_read_b128 v[60:63], v75 offset:7168
	s_waitcnt lgkmcnt(1)
	v_mfma_f32_16x16x32_f16 v[84:87], v[30:33], v[56:59], v[84:87]
	v_mfma_f32_16x16x32_f16 v[88:91], v[22:25], v[56:59], v[88:91]
	s_waitcnt lgkmcnt(0)
	v_mfma_f32_16x16x32_f16 v[84:87], v[34:37], v[60:63], v[84:87]
	v_mfma_f32_16x16x32_f16 v[88:91], v[26:29], v[60:63], v[88:91]
	ds_read_b128 v[44:47], v75 offset:2048
	ds_read_b128 v[68:71], v75 offset:3072
	s_nop 7
	v_exp_f32_e32 v94, v86
	v_exp_f32_e32 v95, v90
	v_exp_f32_e32 v96, v84
	v_exp_f32_e32 v97, v88
	v_exp_f32_e32 v98, v85
	v_exp_f32_e32 v99, v89
	v_pk_add_f32 v[100:101], v[94:95], 1.0 op_sel_hi:[1,0]
	v_pk_fma_f32 v[102:103], v[94:95], s[8:9], v[92:93] op_sel_hi:[1,0,0]
	v_pk_fma_f32 v[100:101], v[96:97], v[100:101], v[100:101]
	v_pk_fma_f32 v[104:105], v[100:101], v[98:99], v[100:101]
	v_rcp_f32_e32 v104, v104
	v_rcp_f32_e32 v105, v105
	v_pk_fma_f32 v[102:103], v[102:103], v[98:99], v[102:103]
	v_pk_fma_f32 v[102:103], v[64:65], v[100:101], v[102:103]
	v_exp_f32_e32 v106, v87
	v_pk_mul_f32 v[64:65], v[102:103], v[104:105]
	v_exp_f32_e32 v108, v64
	v_exp_f32_e32 v109, v65
	v_exp_f32_e32 v107, v91
	v_pk_add_f32 v[110:111], v[108:109], 1.0 op_sel_hi:[1,0]
	v_pk_fma_f32 v[110:111], v[110:111], v[106:107], v[110:111]
	v_rcp_f32_e32 v110, v110
	v_rcp_f32_e32 v111, v111
	v_pk_add_f32 v[112:113], v[108:109], -1.0 op_sel_hi:[1,0]
	v_pk_mul_f32 v[112:113], v[112:113], v[110:111]
	v_cvt_pk_f16_f32 v114, v112, v113
	ds_write_b32 v81, v114 offset:4096
	s_waitcnt lgkmcnt(1)
	v_mfma_f32_16x16x32_f16 v[84:87], v[2:5], v[44:47], v[18:21]
	v_mfma_f32_16x16x32_f16 v[88:91], v[14:17], v[44:47], v[38:41]
	v_mfma_f32_16x16x32_f16 v[84:87], v[6:9], v[68:71], v[84:87]
	v_mfma_f32_16x16x32_f16 v[88:91], v[10:13], v[68:71], v[88:91]
	s_waitcnt lgkmcnt(0)
	s_barrier
	ds_read_b128 v[56:59], v75 offset:4096
	ds_read_b128 v[60:63], v75 offset:5120
	s_waitcnt lgkmcnt(1)
	v_mfma_f32_16x16x32_f16 v[84:87], v[30:33], v[56:59], v[84:87]
	v_mfma_f32_16x16x32_f16 v[88:91], v[22:25], v[56:59], v[88:91]
	s_waitcnt lgkmcnt(0)
	v_mfma_f32_16x16x32_f16 v[84:87], v[34:37], v[60:63], v[84:87]
	v_mfma_f32_16x16x32_f16 v[88:91], v[26:29], v[60:63], v[88:91]
	ds_read_b128 v[44:47], v75 offset:0
	ds_read_b128 v[68:71], v75 offset:1024
	s_nop 7
	v_exp_f32_e32 v94, v86
	v_exp_f32_e32 v95, v90
	v_exp_f32_e32 v96, v84
	v_exp_f32_e32 v97, v88
	v_exp_f32_e32 v98, v85
	v_exp_f32_e32 v99, v89
	v_pk_add_f32 v[100:101], v[94:95], 1.0 op_sel_hi:[1,0]
	v_pk_fma_f32 v[102:103], v[94:95], s[8:9], v[92:93] op_sel_hi:[1,0,0]
	v_pk_fma_f32 v[100:101], v[96:97], v[100:101], v[100:101]
	v_pk_fma_f32 v[104:105], v[100:101], v[98:99], v[100:101]
	v_rcp_f32_e32 v104, v104
	v_rcp_f32_e32 v105, v105
	v_pk_fma_f32 v[102:103], v[102:103], v[98:99], v[102:103]
	v_pk_fma_f32 v[102:103], v[64:65], v[100:101], v[102:103]
	v_exp_f32_e32 v106, v87
	v_pk_mul_f32 v[64:65], v[102:103], v[104:105]
	v_exp_f32_e32 v108, v64
	v_exp_f32_e32 v109, v65
	v_exp_f32_e32 v107, v91
	v_pk_add_f32 v[110:111], v[108:109], 1.0 op_sel_hi:[1,0]
	v_pk_fma_f32 v[110:111], v[110:111], v[106:107], v[110:111]
	v_rcp_f32_e32 v110, v110
	v_rcp_f32_e32 v111, v111
	v_pk_add_f32 v[112:113], v[108:109], -1.0 op_sel_hi:[1,0]
	v_pk_mul_f32 v[112:113], v[112:113], v[110:111]
	v_cvt_pk_f16_f32 v114, v112, v113
	ds_write_b32 v81, v114 offset:6144
	s_waitcnt lgkmcnt(1)
	v_mfma_f32_16x16x32_f16 v[84:87], v[2:5], v[44:47], v[18:21]
	v_mfma_f32_16x16x32_f16 v[88:91], v[14:17], v[44:47], v[38:41]
	v_mfma_f32_16x16x32_f16 v[84:87], v[6:9], v[68:71], v[84:87]
	v_mfma_f32_16x16x32_f16 v[88:91], v[10:13], v[68:71], v[88:91]
	s_waitcnt lgkmcnt(0)
	v_min_f32_e32 v64, 0x42700000, v64
	v_min_f32_e32 v65, 0x42700000, v65
	s_add_u32 s12, s12, 4
	v_add_u32_e32 v124, 16, v124
	s_cmp_lt_u32 s12, 452
	s_cbranch_scc1 .Lcb3_loop
	s_barrier
	ds_read_b128 v[56:59], v75 offset:6144
	ds_read_b128 v[60:63], v75 offset:7168
	s_waitcnt lgkmcnt(0)
	s_waitcnt lgkmcnt(0)
	s_barrier
	s_waitcnt lgkmcnt(0)
	s_endpgm
.Lcb_r0:
	s_barrier
	ds_read_b128 v[44:47], v75 offset:0
	ds_read_b128 v[68:71], v75 offset:1024
	s_waitcnt lgkmcnt(0)
	v_mfma_f32_16x16x32_f16 v[84:87], v[2:5], v[44:47], v[18:21]
	v_mfma_f32_16x16x32_f16 v[88:91], v[14:17], v[44:47], v[38:41]
	v_mfma_f32_16x16x32_f16 v[84:87], v[6:9], v[68:71], v[84:87]
	v_mfma_f32_16x16x32_f16 v[88:91], v[10:13], v[68:71], v[88:91]
	s_barrier
	ds_read_b128 v[56:59], v75 offset:6144
	ds_read_b128 v[60:63], v75 offset:7168
	s_waitcnt lgkmcnt(1)
	v_mfma_f32_16x16x32_f16 v[84:87], v[30:33], v[56:59], v[84:87]
	v_mfma_f32_16x16x32_f16 v[88:91], v[22:25], v[56:59], v[88:91]
	s_waitcnt lgkmcnt(0)
	v_mfma_f32_16x16x32_f16 v[84:87], v[34:37], v[60:63], v[84:87]
	v_mfma_f32_16x16x32_f16 v[88:91], v[26:29], v[60:63], v[88:91]
	ds_read_b128 v[44:47], v75 offset:2048
	ds_read_b128 v[68:71], v75 offset:3072
	s_nop 7
	v_exp_f32_e32 v94, v86
	v_exp_f32_e32 v95, v90
	v_exp_f32_e32 v96, v84
	v_exp_f32_e32 v97, v88
	v_exp_f32_e32 v98, v85
	v_exp_f32_e32 v99, v89
	v_pk_add_f32 v[100:101], v[94:95], 1.0 op_sel_hi:[1,0]
	v_pk_fma_f32 v[102:103], v[94:95], s[8:9], v[92:93] op_sel_hi:[1,0,0]
	v_pk_fma_f32 v[100:101], v[96:97], v[100:101], v[100:101]
	v_pk_fma_f32 v[104:105], v[100:101], v[98:99], v[100:101]
	v_rcp_f32_e32 v104, v104
	v_rcp_f32_e32 v105, v105
	v_pk_fma_f32 v[102:103], v[102:103], v[98:99], v[102:103]
	v_pk_fma_f32 v[102:103], v[64:65], v[100:101], v[102:103]
	v_exp_f32_e32 v106, v87
	v_pk_mul_f32 v[64:65], v[102:103], v[104:105]
	v_exp_f32_e32 v108, v64
	v_exp_f32_e32 v109, v65
	v_exp_f32_e32 v107, v91
	v_pk_add_f32 v[110:111], v[108:109], 1.0 op_sel_hi:[1,0]
	v_pk_fma_f32 v[110:111], v[110:111], v[106:107], v[110:111]
	v_rcp_f32_e32 v110, v110
	v_rcp_f32_e32 v111, v111
	v_pk_add_f32 v[112:113], v[108:109], -1.0 op_sel_hi:[1,0]
	v_pk_mul_f32 v[112:113], v[112:113], v[110:111]
	v_cvt_pk_f16_f32 v114, v112, v113
	ds_write_b32 v81, v114 offset:4096
	s_waitcnt lgkmcnt(1)
	v_mfma_f32_16x16x32_f16 v[84:87], v[2:5], v[44:47], v[18:21]
	v_mfma_f32_16x16x32_f16 v[88:91], v[14:17], v[44:47], v[38:41]
	v_mfma_f32_16x16x32_f16 v[84:87], v[6:9], v[68:71], v[84:87]
	v_mfma_f32_16x16x32_f16 v[88:91], v[10:13], v[68:71], v[88:91]
	s_waitcnt lgkmcnt(0)
	s_barrier
	ds_read_b128 v[56:59], v75 offset:4096
	ds_read_b128 v[60:63], v75 offset:5120
	s_waitcnt lgkmcnt(1)
	v_mfma_f32_16x16x32_f16 v[84:87], v[30:33], v[56:59], v[84:87]
	v_mfma_f32_16x16x32_f16 v[88:91], v[22:25], v[56:59], v[88:91]
	s_waitcnt lgkmcnt(0)
	v_mfma_f32_16x16x32_f16 v[84:87], v[34:37], v[60:63], v[84:87]
	v_mfma_f32_16x16x32_f16 v[88:91], v[26:29], v[60:63], v[88:91]
	ds_read_b128 v[44:47], v75 offset:0
	ds_read_b128 v[68:71], v75 offset:1024
	v_mfma_f32_16x16x32_f16 v[50:53], v[116:119], v[56:59], 0
	s_nop 7
	v_exp_f32_e32 v94, v86
	v_exp_f32_e32 v95, v90
	v_exp_f32_e32 v96, v84
	v_exp_f32_e32 v97, v88
	v_exp_f32_e32 v98, v85
	v_exp_f32_e32 v99, v89
	v_add_f32_e32 v125, v50, v51
	v_add_f32_e32 v125, s28, v125
	s_mov_b64 s[16:17], exec
	s_mov_b64 exec, s[30:31]
	ds_write_b32 v74, v125 offset:128
	s_mov_b64 exec, s[16:17]
	v_pk_add_f32 v[100:101], v[94:95], 1.0 op_sel_hi:[1,0]
	v_pk_fma_f32 v[102:103], v[94:95], s[8:9], v[92:93] op_sel_hi:[1,0,0]
	v_pk_fma_f32 v[100:101], v[96:97], v[100:101], v[100:101]
	v_pk_fma_f32 v[104:105], v[100:101], v[98:99], v[100:101]
	v_rcp_f32_e32 v104, v104
	v_rcp_f32_e32 v105, v105
	v_pk_fma_f32 v[102:103], v[102:103], v[98:99], v[102:103]
	v_pk_fma_f32 v[102:103], v[64:65], v[100:101], v[102:103]
	v_exp_f32_e32 v106, v87
	v_pk_mul_f32 v[64:65], v[102:103], v[104:105]
	v_exp_f32_e32 v108, v64
	v_exp_f32_e32 v109, v65
	v_exp_f32_e32 v107, v91
	v_pk_add_f32 v[110:111], v[108:109], 1.0 op_sel_hi:[1,0]
	v_pk_fma_f32 v[110:111], v[110:111], v[106:107], v[110:111]
	v_rcp_f32_e32 v110, v110
	v_rcp_f32_e32 v111, v111
	v_pk_add_f32 v[112:113], v[108:109], -1.0 op_sel_hi:[1,0]
	v_pk_mul_f32 v[112:113], v[112:113], v[110:111]
	v_cvt_pk_f16_f32 v114, v112, v113
	ds_write_b32 v81, v114 offset:6144
	s_waitcnt lgkmcnt(1)
	v_mfma_f32_16x16x32_f16 v[84:87], v[2:5], v[44:47], v[18:21]
	v_mfma_f32_16x16x32_f16 v[88:91], v[14:17], v[44:47], v[38:41]
	v_mfma_f32_16x16x32_f16 v[84:87], v[6:9], v[68:71], v[84:87]
	v_mfma_f32_16x16x32_f16 v[88:91], v[10:13], v[68:71], v[88:91]
	s_waitcnt lgkmcnt(0)
	.p2align	6
.Lcb0_loop:
	s_barrier
	ds_read_b128 v[56:59], v75 offset:6144
	ds_read_b128 v[60:63], v75 offset:7168
	s_waitcnt lgkmcnt(1)
	v_mfma_f32_16x16x32_f16 v[84:87], v[30:33], v[56:59], v[84:87]
	v_mfma_f32_16x16x32_f16 v[88:91], v[22:25], v[56:59], v[88:91]
	s_waitcnt lgkmcnt(0)
	v_mfma_f32_16x16x32_f16 v[84:87], v[34:37], v[60:63], v[84:87]
	v_mfma_f32_16x16x32_f16 v[88:91], v[26:29], v[60:63], v[88:91]
	ds_read_b128 v[44:47], v75 offset:2048
	ds_read_b128 v[68:71], v75 offset:3072
	v_mfma_f32_16x16x32_f16 v[50:53], v[116:119], v[56:59], 0
	s_nop 7
	v_exp_f32_e32 v94, v86
	v_exp_f32_e32 v95, v90
	v_exp_f32_e32 v96, v84
	v_exp_f32_e32 v97, v88
	v_exp_f32_e32 v98, v85
	v_exp_f32_e32 v99, v89
	v_add_f32_e32 v125, v50, v51
	v_add_f32_e32 v125, s28, v125
	s_mov_b64 s[16:17], exec
	s_mov_b64 exec, s[30:31]
	ds_write_b32 v74, v125 offset:0
	s_mov_b64 exec, s[16:17]
	v_pk_add_f32 v[100:101], v[94:95], 1.0 op_sel_hi:[1,0]
	v_pk_fma_f32 v[102:103], v[94:95], s[8:9], v[92:93] op_sel_hi:[1,0,0]
	v_pk_fma_f32 v[100:101], v[96:97], v[100:101], v[100:101]
	v_pk_fma_f32 v[104:105], v[100:101], v[98:99], v[100:101]
	v_rcp_f32_e32 v104, v104
	v_rcp_f32_e32 v105, v105
	v_pk_fma_f32 v[102:103], v[102:103], v[98:99], v[102:103]
	v_pk_fma_f32 v[102:103], v[64:65], v[100:101], v[102:103]
	v_exp_f32_e32 v106, v87
	v_pk_mul_f32 v[64:65], v[102:103], v[104:105]
	v_exp_f32_e32 v108, v64
	v_exp_f32_e32 v109, v65
	v_exp_f32_e32 v107, v91
	v_pk_add_f32 v[110:111], v[108:109], 1.0 op_sel_hi:[1,0]
	v_pk_fma_f32 v[110:111], v[110:111], v[106:107], v[110:111]
	v_rcp_f32_e32 v110, v110
	v_rcp_f32_e32 v111, v111
	v_pk_add_f32 v[112:113], v[108:109], -1.0 op_sel_hi:[1,0]
	v_pk_mul_f32 v[112:113], v[112:113], v[110:111]
	v_cvt_pk_f16_f32 v114, v112, v113
	ds_write_b32 v81, v114 offset:4096
	s_waitcnt lgkmcnt(1)
	v_mfma_f32_16x16x32_f16 v[84:87], v[2:5], v[44:47], v[18:21]
	v_mfma_f32_16x16x32_f16 v[88:91], v[14:17], v[44:47], v[38:41]
	v_mfma_f32_16x16x32_f16 v[84:87], v[6:9], v[68:71], v[84:87]
	v_mfma_f32_16x16x32_f16 v[88:91], v[10:13], v[68:71], v[88:91]
	s_waitcnt lgkmcnt(0)
	s_barrier
	ds_read_b128 v[56:59], v75 offset:4096
	ds_read_b128 v[60:63], v75 offset:5120
	s_waitcnt lgkmcnt(1)
	v_mfma_f32_16x16x32_f16 v[84:87], v[30:33], v[56:59], v[84:87]
	v_mfma_f32_16x16x32_f16 v[88:91], v[22:25], v[56:59], v[88:91]
	s_waitcnt lgkmcnt(0)
	v_mfma_f32_16x16x32_f16 v[84:87], v[34:37], v[60:63], v[84:87]
	v_mfma_f32_16x16x32_f16 v[88:91], v[26:29], v[60:63], v[88:91]
	ds_read_b128 v[44:47], v75 offset:0
	ds_read_b128 v[68:71], v75 offset:1024
	v_mfma_f32_16x16x32_f16 v[50:53], v[116:119], v[56:59], 0
	s_nop 7
	v_exp_f32_e32 v94, v86
	v_exp_f32_e32 v95, v90
	v_exp_f32_e32 v96, v84
	v_exp_f32_e32 v97, v88
	v_exp_f32_e32 v98, v85
	v_exp_f32_e32 v99, v89
	v_add_f32_e32 v125, v50, v51
	v_add_f32_e32 v125, s28, v125
	s_mov_b64 s[16:17], exec
	s_mov_b64 exec, s[30:31]
	ds_write_b32 v74, v125 offset:128
	s_mov_b64 exec, s[16:17]
	v_pk_add_f32 v[100:101], v[94:95], 1.0 op_sel_hi:[1,0]
	v_pk_fma_f32 v[102:103], v[94:95], s[8:9], v[92:93] op_sel_hi:[1,0,0]
	v_pk_fma_f32 v[100:101], v[96:97], v[100:101], v[100:101]
	v_pk_fma_f32 v[104:105], v[100:101], v[98:99], v[100:101]
	v_rcp_f32_e32 v104, v104
	v_rcp_f32_e32 v105, v105
	v_pk_fma_f32 v[102:103], v[102:103], v[98:99], v[102:103]
	v_pk_fma_f32 v[102:103], v[64:65], v[100:101], v[102:103]
	v_exp_f32_e32 v106, v87
	v_pk_mul_f32 v[64:65], v[102:103], v[104:105]
	v_exp_f32_e32 v108, v64
	v_exp_f32_e32 v109, v65
	v_exp_f32_e32 v107, v91
	v_pk_add_f32 v[110:111], v[108:109], 1.0 op_sel_hi:[1,0]
	v_pk_fma_f32 v[110:111], v[110:111], v[106:107], v[110:111]
	v_rcp_f32_e32 v110, v110
	v_rcp_f32_e32 v111, v111
	v_pk_add_f32 v[112:113], v[108:109], -1.0 op_sel_hi:[1,0]
	v_pk_mul_f32 v[112:113], v[112:113], v[110:111]
	v_cvt_pk_f16_f32 v114, v112, v113
	ds_write_b32 v81, v114 offset:6144
	s_waitcnt lgkmcnt(1)
	v_mfma_f32_16x16x32_f16 v[84:87], v[2:5], v[44:47], v[18:21]
	v_mfma_f32_16x16x32_f16 v[88:91], v[14:17], v[44:47], v[38:41]
	v_mfma_f32_16x16x32_f16 v[84:87], v[6:9], v[68:71], v[84:87]
	v_mfma_f32_16x16x32_f16 v[88:91], v[10:13], v[68:71], v[88:91]
	s_waitcnt lgkmcnt(0)
	s_barrier
	ds_read_b128 v[56:59], v75 offset:6144
	ds_read_b128 v[60:63], v75 offset:7168
	s_waitcnt lgkmcnt(1)
	v_mfma_f32_16x16x32_f16 v[84:87], v[30:33], v[56:59], v[84:87]
	v_mfma_f32_16x16x32_f16 v[88:91], v[22:25], v[56:59], v[88:91]
	s_waitcnt lgkmcnt(0)
	v_mfma_f32_16x16x32_f16 v[84:87], v[34:37], v[60:63], v[84:87]
	v_mfma_f32_16x16x32_f16 v[88:91], v[26:29], v[60:63], v[88:91]
	ds_read_b128 v[44:47], v75 offset:2048
	ds_read_b128 v[68:71], v75 offset:3072
	v_mfma_f32_16x16x32_f16 v[50:53], v[116:119], v[56:59], 0
	s_nop 7
	v_exp_f32_e32 v94, v86
	v_exp_f32_e32 v95, v90
	v_exp_f32_e32 v96, v84
	v_exp_f32_e32 v97, v88
	v_exp_f32_e32 v98, v85
	v_exp_f32_e32 v99, v89
	v_add_f32_e32 v125, v50, v51
	v_add_f32_e32 v125, s28, v125
	s_mov_b64 s[16:17], exec
	s_mov_b64 exec, s[30:31]
	ds_write_b32 v74, v125 offset:0
	s_mov_b64 exec, s[16:17]
	v_pk_add_f32 v[100:101], v[94:95], 1.0 op_sel_hi:[1,0]
	v_pk_fma_f32 v[102:103], v[94:95], s[8:9], v[92:93] op_sel_hi:[1,0,0]
	v_pk_fma_f32 v[100:101], v[96:97], v[100:101], v[100:101]
	v_pk_fma_f32 v[104:105], v[100:101], v[98:99], v[100:101]
	v_rcp_f32_e32 v104, v104
	v_rcp_f32_e32 v105, v105
	v_pk_fma_f32 v[102:103], v[102:103], v[98:99], v[102:103]
	v_pk_fma_f32 v[102:103], v[64:65], v[100:101], v[102:103]
	v_exp_f32_e32 v106, v87
	v_pk_mul_f32 v[64:65], v[102:103], v[104:105]
	v_exp_f32_e32 v108, v64
	v_exp_f32_e32 v109, v65
	v_exp_f32_e32 v107, v91
	v_pk_add_f32 v[110:111], v[108:109], 1.0 op_sel_hi:[1,0]
	v_pk_fma_f32 v[110:111], v[110:111], v[106:107], v[110:111]
	v_rcp_f32_e32 v110, v110
	v_rcp_f32_e32 v111, v111
	v_pk_add_f32 v[112:113], v[108:109], -1.0 op_sel_hi:[1,0]
	v_pk_mul_f32 v[112:113], v[112:113], v[110:111]
	v_cvt_pk_f16_f32 v114, v112, v113
	ds_write_b32 v81, v114 offset:4096
	s_waitcnt lgkmcnt(1)
	v_mfma_f32_16x16x32_f16 v[84:87], v[2:5], v[44:47], v[18:21]
	v_mfma_f32_16x16x32_f16 v[88:91], v[14:17], v[44:47], v[38:41]
	v_mfma_f32_16x16x32_f16 v[84:87], v[6:9], v[68:71], v[84:87]
	v_mfma_f32_16x16x32_f16 v[88:91], v[10:13], v[68:71], v[88:91]
	s_waitcnt lgkmcnt(0)
	s_barrier
	ds_read_b128 v[56:59], v75 offset:4096
	ds_read_b128 v[60:63], v75 offset:5120
	s_waitcnt lgkmcnt(1)
	v_mfma_f32_16x16x32_f16 v[84:87], v[30:33], v[56:59], v[84:87]
	v_mfma_f32_16x16x32_f16 v[88:91], v[22:25], v[56:59], v[88:91]
	s_waitcnt lgkmcnt(0)
	v_mfma_f32_16x16x32_f16 v[84:87], v[34:37], v[60:63], v[84:87]
	v_mfma_f32_16x16x32_f16 v[88:91], v[26:29], v[60:63], v[88:91]
	ds_read_b128 v[44:47], v75 offset:0
	ds_read_b128 v[68:71], v75 offset:1024
	v_mfma_f32_16x16x32_f16 v[50:53], v[116:119], v[56:59], 0
	s_nop 7
	v_exp_f32_e32 v94, v86
	v_exp_f32_e32 v95, v90
	v_exp_f32_e32 v96, v84
	v_exp_f32_e32 v97, v88
	v_exp_f32_e32 v98, v85
	v_exp_f32_e32 v99, v89
	v_add_f32_e32 v125, v50, v51
	v_add_f32_e32 v125, s28, v125
	s_mov_b64 s[16:17], exec
	s_mov_b64 exec, s[30:31]
	ds_write_b32 v74, v125 offset:128
	s_mov_b64 exec, s[16:17]
	v_pk_add_f32 v[100:101], v[94:95], 1.0 op_sel_hi:[1,0]
	v_pk_fma_f32 v[102:103], v[94:95], s[8:9], v[92:93] op_sel_hi:[1,0,0]
	v_pk_fma_f32 v[100:101], v[96:97], v[100:101], v[100:101]
	v_pk_fma_f32 v[104:105], v[100:101], v[98:99], v[100:101]
	v_rcp_f32_e32 v104, v104
	v_rcp_f32_e32 v105, v105
	v_pk_fma_f32 v[102:103], v[102:103], v[98:99], v[102:103]
	v_pk_fma_f32 v[102:103], v[64:65], v[100:101], v[102:103]
	v_exp_f32_e32 v106, v87
	v_pk_mul_f32 v[64:65], v[102:103], v[104:105]
	v_exp_f32_e32 v108, v64
	v_exp_f32_e32 v109, v65
	v_exp_f32_e32 v107, v91
	v_pk_add_f32 v[110:111], v[108:109], 1.0 op_sel_hi:[1,0]
	v_pk_fma_f32 v[110:111], v[110:111], v[106:107], v[110:111]
	v_rcp_f32_e32 v110, v110
	v_rcp_f32_e32 v111, v111
	v_pk_add_f32 v[112:113], v[108:109], -1.0 op_sel_hi:[1,0]
	v_pk_mul_f32 v[112:113], v[112:113], v[110:111]
	v_cvt_pk_f16_f32 v114, v112, v113
	ds_write_b32 v81, v114 offset:6144
	s_waitcnt lgkmcnt(1)
	v_mfma_f32_16x16x32_f16 v[84:87], v[2:5], v[44:47], v[18:21]
	v_mfma_f32_16x16x32_f16 v[88:91], v[14:17], v[44:47], v[38:41]
	v_mfma_f32_16x16x32_f16 v[84:87], v[6:9], v[68:71], v[84:87]
	v_mfma_f32_16x16x32_f16 v[88:91], v[10:13], v[68:71], v[88:91]
	s_waitcnt lgkmcnt(0)
	v_min_f32_e32 v64, 0x42700000, v64
	v_min_f32_e32 v65, 0x42700000, v65
	s_add_u32 s12, s12, 4
	v_add_u32_e32 v124, 16, v124
	s_cmp_lt_u32 s12, 452
	s_cbranch_scc1 .Lcb0_loop
	s_barrier
	ds_read_b128 v[56:59], v75 offset:6144
	ds_read_b128 v[60:63], v75 offset:7168
	s_waitcnt lgkmcnt(0)
	v_mfma_f32_16x16x32_f16 v[50:53], v[116:119], v[56:59], 0
	s_nop 7
	v_add_f32_e32 v125, v50, v51
	v_add_f32_e32 v125, s28, v125
	s_mov_b64 s[16:17], exec
	s_mov_b64 exec, s[30:31]
	ds_write_b32 v74, v125 offset:0
	s_mov_b64 exec, s[16:17]
	s_waitcnt lgkmcnt(0)
	s_barrier
	s_waitcnt lgkmcnt(0)
	s_endpgm
.Lcb_r1:
	s_barrier
	ds_read_b128 v[44:47], v75 offset:0
	ds_read_b128 v[68:71], v75 offset:1024
	s_waitcnt lgkmcnt(0)
	v_mfma_f32_16x16x32_f16 v[84:87], v[2:5], v[44:47], v[18:21]
	v_mfma_f32_16x16x32_f16 v[88:91], v[14:17], v[44:47], v[38:41]
	v_mfma_f32_16x16x32_f16 v[84:87], v[6:9], v[68:71], v[84:87]
	v_mfma_f32_16x16x32_f16 v[88:91], v[10:13], v[68:71], v[88:91]
	s_barrier
	ds_read_b128 v[56:59], v75 offset:6144
	ds_read_b128 v[60:63], v75 offset:7168
	s_waitcnt lgkmcnt(1)
	v_mfma_f32_16x16x32_f16 v[84:87], v[30:33], v[56:59], v[84:87]
	v_mfma_f32_16x16x32_f16 v[88:91], v[22:25], v[56:59], v[88:91]
	s_waitcnt lgkmcnt(0)
	v_mfma_f32_16x16x32_f16 v[84:87], v[34:37], v[60:63], v[84:87]
	v_mfma_f32_16x16x32_f16 v[88:91], v[26:29], v[60:63], v[88:91]
	ds_read_b128 v[44:47], v75 offset:2048
	ds_read_b128 v[68:71], v75 offset:3072
	s_nop 7
	v_exp_f32_e32 v94, v86
	v_exp_f32_e32 v95, v90
	v_exp_f32_e32 v96, v84
	v_exp_f32_e32 v97, v88
	v_exp_f32_e32 v98, v85
	v_exp_f32_e32 v99, v89
	v_pk_add_f32 v[100:101], v[94:95], 1.0 op_sel_hi:[1,0]
	v_pk_fma_f32 v[102:103], v[94:95], s[8:9], v[92:93] op_sel_hi:[1,0,0]
	v_pk_fma_f32 v[100:101], v[96:97], v[100:101], v[100:101]
	v_pk_fma_f32 v[104:105], v[100:101], v[98:99], v[100:101]
	v_rcp_f32_e32 v104, v104
	v_rcp_f32_e32 v105, v105
	v_pk_fma_f32 v[102:103], v[102:103], v[98:99], v[102:103]
	v_pk_fma_f32 v[102:103], v[64:65], v[100:101], v[102:103]
	v_exp_f32_e32 v106, v87
	v_pk_mul_f32 v[64:65], v[102:103], v[104:105]
	v_exp_f32_e32 v108, v64
	v_exp_f32_e32 v109, v65
	v_exp_f32_e32 v107, v91
	v_pk_add_f32 v[110:111], v[108:109], 1.0 op_sel_hi:[1,0]
	v_pk_fma_f32 v[110:111], v[110:111], v[106:107], v[110:111]
	v_rcp_f32_e32 v110, v110
	v_rcp_f32_e32 v111, v111
	v_pk_add_f32 v[112:113], v[108:109], -1.0 op_sel_hi:[1,0]
	v_pk_mul_f32 v[112:113], v[112:113], v[110:111]
	v_cvt_pk_f16_f32 v114, v112, v113
	ds_write_b32 v81, v114 offset:4096
	s_waitcnt lgkmcnt(1)
	v_mfma_f32_16x16x32_f16 v[84:87], v[2:5], v[44:47], v[18:21]
	v_mfma_f32_16x16x32_f16 v[88:91], v[14:17], v[44:47], v[38:41]
	v_mfma_f32_16x16x32_f16 v[84:87], v[6:9], v[68:71], v[84:87]
	v_mfma_f32_16x16x32_f16 v[88:91], v[10:13], v[68:71], v[88:91]
	s_waitcnt lgkmcnt(0)
	s_barrier
	ds_read_b128 v[56:59], v75 offset:4096
	ds_read_b128 v[60:63], v75 offset:5120
	s_waitcnt lgkmcnt(1)
	v_mfma_f32_16x16x32_f16 v[84:87], v[30:33], v[56:59], v[84:87]
	v_mfma_f32_16x16x32_f16 v[88:91], v[22:25], v[56:59], v[88:91]
	s_waitcnt lgkmcnt(0)
	v_mfma_f32_16x16x32_f16 v[84:87], v[34:37], v[60:63], v[84:87]
	v_mfma_f32_16x16x32_f16 v[88:91], v[26:29], v[60:63], v[88:91]
	ds_read_b128 v[44:47], v75 offset:0
	ds_read_b128 v[68:71], v75 offset:1024
	v_mfma_f32_16x16x32_f16 v[50:53], v[120:123], v[60:63], 0
	s_nop 7
	v_exp_f32_e32 v94, v86
	v_exp_f32_e32 v95, v90
	v_exp_f32_e32 v96, v84
	v_exp_f32_e32 v97, v88
	v_exp_f32_e32 v98, v85
	v_exp_f32_e32 v99, v89
	v_add_f32_e32 v125, v50, v51
	s_mov_b64 s[16:17], exec
	s_mov_b64 exec, s[30:31]
	ds_write_b32 v74, v125 offset:192
	s_mov_b64 exec, s[16:17]
	v_pk_add_f32 v[100:101], v[94:95], 1.0 op_sel_hi:[1,0]
	v_pk_fma_f32 v[102:103], v[94:95], s[8:9], v[92:93] op_sel_hi:[1,0,0]
	v_pk_fma_f32 v[100:101], v[96:97], v[100:101], v[100:101]
	v_pk_fma_f32 v[104:105], v[100:101], v[98:99], v[100:101]
	v_rcp_f32_e32 v104, v104
	v_rcp_f32_e32 v105, v105
	v_pk_fma_f32 v[102:103], v[102:103], v[98:99], v[102:103]
	v_pk_fma_f32 v[102:103], v[64:65], v[100:101], v[102:103]
	v_exp_f32_e32 v106, v87
	v_pk_mul_f32 v[64:65], v[102:103], v[104:105]
	v_exp_f32_e32 v108, v64
	v_exp_f32_e32 v109, v65
	v_exp_f32_e32 v107, v91
	v_pk_add_f32 v[110:111], v[108:109], 1.0 op_sel_hi:[1,0]
	v_pk_fma_f32 v[110:111], v[110:111], v[106:107], v[110:111]
	v_rcp_f32_e32 v110, v110
	v_rcp_f32_e32 v111, v111
	v_pk_add_f32 v[112:113], v[108:109], -1.0 op_sel_hi:[1,0]
	v_pk_mul_f32 v[112:113], v[112:113], v[110:111]
	v_cvt_pk_f16_f32 v114, v112, v113
	ds_write_b32 v81, v114 offset:6144
	s_waitcnt lgkmcnt(1)
	v_mfma_f32_16x16x32_f16 v[84:87], v[2:5], v[44:47], v[18:21]
	v_mfma_f32_16x16x32_f16 v[88:91], v[14:17], v[44:47], v[38:41]
	v_mfma_f32_16x16x32_f16 v[84:87], v[6:9], v[68:71], v[84:87]
	v_mfma_f32_16x16x32_f16 v[88:91], v[10:13], v[68:71], v[88:91]
	s_waitcnt lgkmcnt(0)
	.p2align	6
.Lcb1_loop:
	s_barrier
	ds_read_b128 v[56:59], v75 offset:6144
	ds_read_b128 v[60:63], v75 offset:7168
	s_waitcnt lgkmcnt(1)
	v_mfma_f32_16x16x32_f16 v[84:87], v[30:33], v[56:59], v[84:87]
	v_mfma_f32_16x16x32_f16 v[88:91], v[22:25], v[56:59], v[88:91]
	s_waitcnt lgkmcnt(0)
	v_mfma_f32_16x16x32_f16 v[84:87], v[34:37], v[60:63], v[84:87]
	v_mfma_f32_16x16x32_f16 v[88:91], v[26:29], v[60:63], v[88:91]
	ds_read_b128 v[44:47], v75 offset:2048
	ds_read_b128 v[68:71], v75 offset:3072
	v_mfma_f32_16x16x32_f16 v[50:53], v[120:123], v[60:63], 0
	s_nop 7
	v_exp_f32_e32 v94, v86
	v_exp_f32_e32 v95, v90
	v_exp_f32_e32 v96, v84
	v_exp_f32_e32 v97, v88
	v_exp_f32_e32 v98, v85
	v_exp_f32_e32 v99, v89
	v_add_f32_e32 v125, v50, v51
	s_mov_b64 s[16:17], exec
	s_mov_b64 exec, s[30:31]
	ds_write_b32 v74, v125 offset:64
	s_mov_b64 exec, s[16:17]
	v_pk_add_f32 v[100:101], v[94:95], 1.0 op_sel_hi:[1,0]
	v_pk_fma_f32 v[102:103], v[94:95], s[8:9], v[92:93] op_sel_hi:[1,0,0]
	v_pk_fma_f32 v[100:101], v[96:97], v[100:101], v[100:101]
	v_pk_fma_f32 v[104:105], v[100:101], v[98:99], v[100:101]
	v_rcp_f32_e32 v104, v104
	v_rcp_f32_e32 v105, v105
	v_pk_fma_f32 v[102:103], v[102:103], v[98:99], v[102:103]
	v_pk_fma_f32 v[102:103], v[64:65], v[100:101], v[102:103]
	v_exp_f32_e32 v106, v87
	v_pk_mul_f32 v[64:65], v[102:103], v[104:105]
	v_exp_f32_e32 v108, v64
	v_exp_f32_e32 v109, v65
	v_exp_f32_e32 v107, v91
	v_pk_add_f32 v[110:111], v[108:109], 1.0 op_sel_hi:[1,0]
	v_pk_fma_f32 v[110:111], v[110:111], v[106:107], v[110:111]
	v_rcp_f32_e32 v110, v110
	v_rcp_f32_e32 v111, v111
	v_pk_add_f32 v[112:113], v[108:109], -1.0 op_sel_hi:[1,0]
	v_pk_mul_f32 v[112:113], v[112:113], v[110:111]
	v_cvt_pk_f16_f32 v114, v112, v113
	ds_write_b32 v81, v114 offset:4096
	s_waitcnt lgkmcnt(1)
	v_mfma_f32_16x16x32_f16 v[84:87], v[2:5], v[44:47], v[18:21]
	v_mfma_f32_16x16x32_f16 v[88:91], v[14:17], v[44:47], v[38:41]
	v_mfma_f32_16x16x32_f16 v[84:87], v[6:9], v[68:71], v[84:87]
	v_mfma_f32_16x16x32_f16 v[88:91], v[10:13], v[68:71], v[88:91]
	s_waitcnt lgkmcnt(0)
	s_barrier
	ds_read_b128 v[56:59], v75 offset:4096
	ds_read_b128 v[60:63], v75 offset:5120
	s_waitcnt lgkmcnt(1)
	v_mfma_f32_16x16x32_f16 v[84:87], v[30:33], v[56:59], v[84:87]
	v_mfma_f32_16x16x32_f16 v[88:91], v[22:25], v[56:59], v[88:91]
	s_waitcnt lgkmcnt(0)
	v_mfma_f32_16x16x32_f16 v[84:87], v[34:37], v[60:63], v[84:87]
	v_mfma_f32_16x16x32_f16 v[88:91], v[26:29], v[60:63], v[88:91]
	ds_read_b128 v[44:47], v75 offset:0
	ds_read_b128 v[68:71], v75 offset:1024
	v_mfma_f32_16x16x32_f16 v[50:53], v[120:123], v[60:63], 0
	s_nop 7
	v_exp_f32_e32 v94, v86
	v_exp_f32_e32 v95, v90
	v_exp_f32_e32 v96, v84
	v_exp_f32_e32 v97, v88
	v_exp_f32_e32 v98, v85
	v_exp_f32_e32 v99, v89
	v_add_f32_e32 v125, v50, v51
	s_mov_b64 s[16:17], exec
	s_mov_b64 exec, s[30:31]
	ds_write_b32 v74, v125 offset:192
	s_mov_b64 exec, s[16:17]
	v_pk_add_f32 v[100:101], v[94:95], 1.0 op_sel_hi:[1,0]
	v_pk_fma_f32 v[102:103], v[94:95], s[8:9], v[92:93] op_sel_hi:[1,0,0]
	v_pk_fma_f32 v[100:101], v[96:97], v[100:101], v[100:101]
	v_pk_fma_f32 v[104:105], v[100:101], v[98:99], v[100:101]
	v_rcp_f32_e32 v104, v104
	v_rcp_f32_e32 v105, v105
	v_pk_fma_f32 v[102:103], v[102:103], v[98:99], v[102:103]
	v_pk_fma_f32 v[102:103], v[64:65], v[100:101], v[102:103]
	v_exp_f32_e32 v106, v87
	v_pk_mul_f32 v[64:65], v[102:103], v[104:105]
	v_exp_f32_e32 v108, v64
	v_exp_f32_e32 v109, v65
	v_exp_f32_e32 v107, v91
	v_pk_add_f32 v[110:111], v[108:109], 1.0 op_sel_hi:[1,0]
	v_pk_fma_f32 v[110:111], v[110:111], v[106:107], v[110:111]
	v_rcp_f32_e32 v110, v110
	v_rcp_f32_e32 v111, v111
	v_pk_add_f32 v[112:113], v[108:109], -1.0 op_sel_hi:[1,0]
	v_pk_mul_f32 v[112:113], v[112:113], v[110:111]
	v_cvt_pk_f16_f32 v114, v112, v113
	ds_write_b32 v81, v114 offset:6144
	s_waitcnt lgkmcnt(1)
	v_mfma_f32_16x16x32_f16 v[84:87], v[2:5], v[44:47], v[18:21]
	v_mfma_f32_16x16x32_f16 v[88:91], v[14:17], v[44:47], v[38:41]
	v_mfma_f32_16x16x32_f16 v[84:87], v[6:9], v[68:71], v[84:87]
	v_mfma_f32_16x16x32_f16 v[88:91], v[10:13], v[68:71], v[88:91]
	s_waitcnt lgkmcnt(0)
	s_barrier
	ds_read_b128 v[56:59], v75 offset:6144
	ds_read_b128 v[60:63], v75 offset:7168
	s_waitcnt lgkmcnt(1)
	v_mfma_f32_16x16x32_f16 v[84:87], v[30:33], v[56:59], v[84:87]
	v_mfma_f32_16x16x32_f16 v[88:91], v[22:25], v[56:59], v[88:91]
	s_waitcnt lgkmcnt(0)
	v_mfma_f32_16x16x32_f16 v[84:87], v[34:37], v[60:63], v[84:87]
	v_mfma_f32_16x16x32_f16 v[88:91], v[26:29], v[60:63], v[88:91]
	ds_read_b128 v[44:47], v75 offset:2048
	ds_read_b128 v[68:71], v75 offset:3072
	v_mfma_f32_16x16x32_f16 v[50:53], v[120:123], v[60:63], 0
	s_nop 7
	v_exp_f32_e32 v94, v86
	v_exp_f32_e32 v95, v90
	v_exp_f32_e32 v96, v84
	v_exp_f32_e32 v97, v88
	v_exp_f32_e32 v98, v85
	v_exp_f32_e32 v99, v89
	v_add_f32_e32 v125, v50, v51
	s_mov_b64 s[16:17], exec
	s_mov_b64 exec, s[30:31]
	ds_write_b32 v74, v125 offset:64
	s_mov_b64 exec, s[16:17]
	v_pk_add_f32 v[100:101], v[94:95], 1.0 op_sel_hi:[1,0]
	v_pk_fma_f32 v[102:103], v[94:95], s[8:9], v[92:93] op_sel_hi:[1,0,0]
	v_pk_fma_f32 v[100:101], v[96:97], v[100:101], v[100:101]
	v_pk_fma_f32 v[104:105], v[100:101], v[98:99], v[100:101]
	v_rcp_f32_e32 v104, v104
	v_rcp_f32_e32 v105, v105
	v_pk_fma_f32 v[102:103], v[102:103], v[98:99], v[102:103]
	v_pk_fma_f32 v[102:103], v[64:65], v[100:101], v[102:103]
	v_exp_f32_e32 v106, v87
	v_pk_mul_f32 v[64:65], v[102:103], v[104:105]
	v_exp_f32_e32 v108, v64
	v_exp_f32_e32 v109, v65
	v_exp_f32_e32 v107, v91
	v_pk_add_f32 v[110:111], v[108:109], 1.0 op_sel_hi:[1,0]
	v_pk_fma_f32 v[110:111], v[110:111], v[106:107], v[110:111]
	v_rcp_f32_e32 v110, v110
	v_rcp_f32_e32 v111, v111
	v_pk_add_f32 v[112:113], v[108:109], -1.0 op_sel_hi:[1,0]
	v_pk_mul_f32 v[112:113], v[112:113], v[110:111]
	v_cvt_pk_f16_f32 v114, v112, v113
	ds_write_b32 v81, v114 offset:4096
	s_waitcnt lgkmcnt(1)
	v_mfma_f32_16x16x32_f16 v[84:87], v[2:5], v[44:47], v[18:21]
	v_mfma_f32_16x16x32_f16 v[88:91], v[14:17], v[44:47], v[38:41]
	v_mfma_f32_16x16x32_f16 v[84:87], v[6:9], v[68:71], v[84:87]
	v_mfma_f32_16x16x32_f16 v[88:91], v[10:13], v[68:71], v[88:91]
	s_waitcnt lgkmcnt(0)
	s_barrier
	ds_read_b128 v[56:59], v75 offset:4096
	ds_read_b128 v[60:63], v75 offset:5120
	s_waitcnt lgkmcnt(1)
	v_mfma_f32_16x16x32_f16 v[84:87], v[30:33], v[56:59], v[84:87]
	v_mfma_f32_16x16x32_f16 v[88:91], v[22:25], v[56:59], v[88:91]
	s_waitcnt lgkmcnt(0)
	v_mfma_f32_16x16x32_f16 v[84:87], v[34:37], v[60:63], v[84:87]
	v_mfma_f32_16x16x32_f16 v[88:91], v[26:29], v[60:63], v[88:91]
	ds_read_b128 v[44:47], v75 offset:0
	ds_read_b128 v[68:71], v75 offset:1024
	v_mfma_f32_16x16x32_f16 v[50:53], v[120:123], v[60:63], 0
	s_nop 7
	v_exp_f32_e32 v94, v86
	v_exp_f32_e32 v95, v90
	v_exp_f32_e32 v96, v84
	v_exp_f32_e32 v97, v88
	v_exp_f32_e32 v98, v85
	v_exp_f32_e32 v99, v89
	v_add_f32_e32 v125, v50, v51
	s_mov_b64 s[16:17], exec
	s_mov_b64 exec, s[30:31]
	ds_write_b32 v74, v125 offset:192
	s_mov_b64 exec, s[16:17]
	v_pk_add_f32 v[100:101], v[94:95], 1.0 op_sel_hi:[1,0]
	v_pk_fma_f32 v[102:103], v[94:95], s[8:9], v[92:93] op_sel_hi:[1,0,0]
	v_pk_fma_f32 v[100:101], v[96:97], v[100:101], v[100:101]
	v_pk_fma_f32 v[104:105], v[100:101], v[98:99], v[100:101]
	v_rcp_f32_e32 v104, v104
	v_rcp_f32_e32 v105, v105
	v_pk_fma_f32 v[102:103], v[102:103], v[98:99], v[102:103]
	v_pk_fma_f32 v[102:103], v[64:65], v[100:101], v[102:103]
	v_exp_f32_e32 v106, v87
	v_pk_mul_f32 v[64:65], v[102:103], v[104:105]
	v_exp_f32_e32 v108, v64
	v_exp_f32_e32 v109, v65
	v_exp_f32_e32 v107, v91
	v_pk_add_f32 v[110:111], v[108:109], 1.0 op_sel_hi:[1,0]
	v_pk_fma_f32 v[110:111], v[110:111], v[106:107], v[110:111]
	v_rcp_f32_e32 v110, v110
	v_rcp_f32_e32 v111, v111
	v_pk_add_f32 v[112:113], v[108:109], -1.0 op_sel_hi:[1,0]
	v_pk_mul_f32 v[112:113], v[112:113], v[110:111]
	v_cvt_pk_f16_f32 v114, v112, v113
	ds_write_b32 v81, v114 offset:6144
	s_waitcnt lgkmcnt(1)
	v_mfma_f32_16x16x32_f16 v[84:87], v[2:5], v[44:47], v[18:21]
	v_mfma_f32_16x16x32_f16 v[88:91], v[14:17], v[44:47], v[38:41]
	v_mfma_f32_16x16x32_f16 v[84:87], v[6:9], v[68:71], v[84:87]
	v_mfma_f32_16x16x32_f16 v[88:91], v[10:13], v[68:71], v[88:91]
	s_waitcnt lgkmcnt(0)
	v_min_f32_e32 v64, 0x42700000, v64
	v_min_f32_e32 v65, 0x42700000, v65
	s_add_u32 s12, s12, 4
	v_add_u32_e32 v124, 16, v124
	s_cmp_lt_u32 s12, 452
	s_cbranch_scc1 .Lcb1_loop
	s_barrier
	ds_read_b128 v[56:59], v75 offset:6144
	ds_read_b128 v[60:63], v75 offset:7168
	s_waitcnt lgkmcnt(0)
	v_mfma_f32_16x16x32_f16 v[50:53], v[120:123], v[60:63], 0
	s_nop 7
	v_add_f32_e32 v125, v50, v51
	s_mov_b64 s[16:17], exec
	s_mov_b64 exec, s[30:31]
	ds_write_b32 v74, v125 offset:64
	s_mov_b64 exec, s[16:17]
	s_waitcnt lgkmcnt(0)
	s_barrier
	s_waitcnt lgkmcnt(0)
	s_endpgm
.Lcb_r2:
	s_barrier
	ds_read_b128 v[44:47], v75 offset:0
	ds_read_b128 v[68:71], v75 offset:1024
	s_waitcnt lgkmcnt(0)
	v_mfma_f32_16x16x32_f16 v[84:87], v[2:5], v[44:47], v[18:21]
	v_mfma_f32_16x16x32_f16 v[88:91], v[14:17], v[44:47], v[38:41]
	v_mfma_f32_16x16x32_f16 v[84:87], v[6:9], v[68:71], v[84:87]
	v_mfma_f32_16x16x32_f16 v[88:91], v[10:13], v[68:71], v[88:91]
	s_barrier
	ds_read_b128 v[56:59], v75 offset:6144
	ds_read_b128 v[60:63], v75 offset:7168
	s_waitcnt lgkmcnt(1)
	v_mfma_f32_16x16x32_f16 v[84:87], v[30:33], v[56:59], v[84:87]
	v_mfma_f32_16x16x32_f16 v[88:91], v[22:25], v[56:59], v[88:91]
	s_waitcnt lgkmcnt(0)
	v_mfma_f32_16x16x32_f16 v[84:87], v[34:37], v[60:63], v[84:87]
	v_mfma_f32_16x16x32_f16 v[88:91], v[26:29], v[60:63], v[88:91]
	ds_read_b128 v[44:47], v75 offset:2048
	ds_read_b128 v[68:71], v75 offset:3072
	s_nop 7
	v_exp_f32_e32 v94, v86
	v_exp_f32_e32 v95, v90
	v_exp_f32_e32 v96, v84
	v_exp_f32_e32 v97, v88
	v_exp_f32_e32 v98, v85
	v_exp_f32_e32 v99, v89
	v_pk_add_f32 v[100:101], v[94:95], 1.0 op_sel_hi:[1,0]
	v_pk_fma_f32 v[102:103], v[94:95], s[8:9], v[92:93] op_sel_hi:[1,0,0]
	v_pk_fma_f32 v[100:101], v[96:97], v[100:101], v[100:101]
	v_pk_fma_f32 v[104:105], v[100:101], v[98:99], v[100:101]
	v_rcp_f32_e32 v104, v104
	v_rcp_f32_e32 v105, v105
	v_pk_fma_f32 v[102:103], v[102:103], v[98:99], v[102:103]
	v_pk_fma_f32 v[102:103], v[64:65], v[100:101], v[102:103]
	v_exp_f32_e32 v106, v87
	v_pk_mul_f32 v[64:65], v[102:103], v[104:105]
	v_exp_f32_e32 v108, v64
	v_exp_f32_e32 v109, v65
	v_exp_f32_e32 v107, v91
	v_pk_add_f32 v[110:111], v[108:109], 1.0 op_sel_hi:[1,0]
	v_pk_fma_f32 v[110:111], v[110:111], v[106:107], v[110:111]
	v_rcp_f32_e32 v110, v110
	v_rcp_f32_e32 v111, v111
	v_pk_add_f32 v[112:113], v[108:109], -1.0 op_sel_hi:[1,0]
	v_pk_mul_f32 v[112:113], v[112:113], v[110:111]
	v_cvt_pk_f16_f32 v114, v112, v113
	ds_write_b32 v81, v114 offset:4096
	s_waitcnt lgkmcnt(1)
	v_mfma_f32_16x16x32_f16 v[84:87], v[2:5], v[44:47], v[18:21]
	v_mfma_f32_16x16x32_f16 v[88:91], v[14:17], v[44:47], v[38:41]
	v_mfma_f32_16x16x32_f16 v[84:87], v[6:9], v[68:71], v[84:87]
	v_mfma_f32_16x16x32_f16 v[88:91], v[10:13], v[68:71], v[88:91]
	s_waitcnt lgkmcnt(0)
	s_barrier
	ds_read_b128 v[56:59], v75 offset:4096
	ds_read_b128 v[60:63], v75 offset:5120
	s_waitcnt lgkmcnt(1)
	v_mfma_f32_16x16x32_f16 v[84:87], v[30:33], v[56:59], v[84:87]
	v_mfma_f32_16x16x32_f16 v[88:91], v[22:25], v[56:59], v[88:91]
	s_waitcnt lgkmcnt(0)
	v_mfma_f32_16x16x32_f16 v[84:87], v[34:37], v[60:63], v[84:87]
	v_mfma_f32_16x16x32_f16 v[88:91], v[26:29], v[60:63], v[88:91]
	ds_read_b128 v[44:47], v75 offset:0
	ds_read_b128 v[68:71], v75 offset:1024
	s_nop 7
	v_exp_f32_e32 v94, v86
	v_exp_f32_e32 v95, v90
	v_exp_f32_e32 v96, v84
	v_exp_f32_e32 v97, v88
	v_exp_f32_e32 v98, v85
	v_exp_f32_e32 v99, v89
	v_pk_add_f32 v[100:101], v[94:95], 1.0 op_sel_hi:[1,0]
	v_pk_fma_f32 v[102:103], v[94:95], s[8:9], v[92:93] op_sel_hi:[1,0,0]
	v_pk_fma_f32 v[100:101], v[96:97], v[100:101], v[100:101]
	v_pk_fma_f32 v[104:105], v[100:101], v[98:99], v[100:101]
	v_rcp_f32_e32 v104, v104
	v_rcp_f32_e32 v105, v105
	v_pk_fma_f32 v[102:103], v[102:103], v[98:99], v[102:103]
	v_pk_fma_f32 v[102:103], v[64:65], v[100:101], v[102:103]
	v_exp_f32_e32 v106, v87
	v_pk_mul_f32 v[64:65], v[102:103], v[104:105]
	v_exp_f32_e32 v108, v64
	v_exp_f32_e32 v109, v65
	v_exp_f32_e32 v107, v91
	v_pk_add_f32 v[110:111], v[108:109], 1.0 op_sel_hi:[1,0]
	v_pk_fma_f32 v[110:111], v[110:111], v[106:107], v[110:111]
	v_rcp_f32_e32 v110, v110
	v_rcp_f32_e32 v111, v111
	v_pk_add_f32 v[112:113], v[108:109], -1.0 op_sel_hi:[1,0]
	v_pk_mul_f32 v[112:113], v[112:113], v[110:111]
	v_cvt_pk_f16_f32 v114, v112, v113
	ds_write_b32 v81, v114 offset:6144
	s_waitcnt lgkmcnt(1)
	v_mfma_f32_16x16x32_f16 v[84:87], v[2:5], v[44:47], v[18:21]
	v_mfma_f32_16x16x32_f16 v[88:91], v[14:17], v[44:47], v[38:41]
	v_mfma_f32_16x16x32_f16 v[84:87], v[6:9], v[68:71], v[84:87]
	v_mfma_f32_16x16x32_f16 v[88:91], v[10:13], v[68:71], v[88:91]
	s_waitcnt lgkmcnt(0)
	.p2align	6
.Lcb2_loop:
	s_barrier
	ds_read_b32 v125, v74 offset:128
	ds_read_b32 v126, v74 offset:192
	ds_read_b128 v[56:59], v75 offset:6144
	ds_read_b128 v[60:63], v75 offset:7168
	s_waitcnt lgkmcnt(2)
	v_add_f32_e32 v125, v125, v126
	v_mul_f32_e32 v126, 0x3fb8aa3b, v125
	v_exp_f32_e32 v126, v126
	v_cmp_lt_f32_e32 vcc, 0, v125
	v_mul_f32_e32 v125, 0x3f867d5f, v125
	v_fma_f32 v126, v126, v72, v73
	s_nop 0
	v_cndmask_b32_e32 v125, v126, v125, vcc
	s_mov_b64 s[16:17], exec
	s_mov_b64 exec, s[30:31]
	global_store_dword v124, v125, s[26:27] offset:0
	s_mov_b64 exec, s[16:17]
	s_waitcnt lgkmcnt(1)
	v_mfma_f32_16x16x32_f16 v[84:87], v[30:33], v[56:59], v[84:87]
	v_mfma_f32_16x16x32_f16 v[88:91], v[22:25], v[56:59], v[88:91]
	s_waitcnt lgkmcnt(0)
	v_mfma_f32_16x16x32_f16 v[84:87], v[34:37], v[60:63], v[84:87]
	v_mfma_f32_16x16x32_f16 v[88:91], v[26:29], v[60:63], v[88:91]
	ds_read_b128 v[44:47], v75 offset:2048
	ds_read_b128 v[68:71], v75 offset:3072
	s_nop 7
	v_exp_f32_e32 v94, v86
	v_exp_f32_e32 v95, v90
	v_exp_f32_e32 v96, v84
	v_exp_f32_e32 v97, v88
	v_exp_f32_e32 v98, v85
	v_exp_f32_e32 v99, v89
	v_pk_add_f32 v[100:101], v[94:95], 1.0 op_sel_hi:[1,0]
	v_pk_fma_f32 v[102:103], v[94:95], s[8:9], v[92:93] op_sel_hi:[1,0,0]
	v_pk_fma_f32 v[100:101], v[96:97], v[100:101], v[100:101]
	v_pk_fma_f32 v[104:105], v[100:101], v[98:99], v[100:101]
	v_rcp_f32_e32 v104, v104
	v_rcp_f32_e32 v105, v105
	v_pk_fma_f32 v[102:103], v[102:103], v[98:99], v[102:103]
	v_pk_fma_f32 v[102:103], v[64:65], v[100:101], v[102:103]
	v_exp_f32_e32 v106, v87
	v_pk_mul_f32 v[64:65], v[102:103], v[104:105]
	v_exp_f32_e32 v108, v64
	v_exp_f32_e32 v109, v65
	v_exp_f32_e32 v107, v91
	v_pk_add_f32 v[110:111], v[108:109], 1.0 op_sel_hi:[1,0]
	v_pk_fma_f32 v[110:111], v[110:111], v[106:107], v[110:111]
	v_rcp_f32_e32 v110, v110
	v_rcp_f32_e32 v111, v111
	v_pk_add_f32 v[112:113], v[108:109], -1.0 op_sel_hi:[1,0]
	v_pk_mul_f32 v[112:113], v[112:113], v[110:111]
	v_cvt_pk_f16_f32 v114, v112, v113
	ds_write_b32 v81, v114 offset:4096
	s_waitcnt lgkmcnt(1)
	v_mfma_f32_16x16x32_f16 v[84:87], v[2:5], v[44:47], v[18:21]
	v_mfma_f32_16x16x32_f16 v[88:91], v[14:17], v[44:47], v[38:41]
	v_mfma_f32_16x16x32_f16 v[84:87], v[6:9], v[68:71], v[84:87]
	v_mfma_f32_16x16x32_f16 v[88:91], v[10:13], v[68:71], v[88:91]
	s_waitcnt lgkmcnt(0)
	s_barrier
	ds_read_b32 v125, v74 offset:0
	ds_read_b32 v126, v74 offset:64
	ds_read_b128 v[56:59], v75 offset:4096
	ds_read_b128 v[60:63], v75 offset:5120
	s_waitcnt lgkmcnt(2)
	v_add_f32_e32 v125, v125, v126
	v_mul_f32_e32 v126, 0x3fb8aa3b, v125
	v_exp_f32_e32 v126, v126
	v_cmp_lt_f32_e32 vcc, 0, v125
	v_mul_f32_e32 v125, 0x3f867d5f, v125
	v_fma_f32 v126, v126, v72, v73
	s_nop 0
	v_cndmask_b32_e32 v125, v126, v125, vcc
	s_mov_b64 s[16:17], exec
	s_mov_b64 exec, s[30:31]
	global_store_dword v124, v125, s[26:27] offset:4
	s_mov_b64 exec, s[16:17]
	s_waitcnt lgkmcnt(1)
	v_mfma_f32_16x16x32_f16 v[84:87], v[30:33], v[56:59], v[84:87]
	v_mfma_f32_16x16x32_f16 v[88:91], v[22:25], v[56:59], v[88:91]
	s_waitcnt lgkmcnt(0)
	v_mfma_f32_16x16x32_f16 v[84:87], v[34:37], v[60:63], v[84:87]
	v_mfma_f32_16x16x32_f16 v[88:91], v[26:29], v[60:63], v[88:91]
	ds_read_b128 v[44:47], v75 offset:0
	ds_read_b128 v[68:71], v75 offset:1024
	s_nop 7
	v_exp_f32_e32 v94, v86
	v_exp_f32_e32 v95, v90
	v_exp_f32_e32 v96, v84
	v_exp_f32_e32 v97, v88
	v_exp_f32_e32 v98, v85
	v_exp_f32_e32 v99, v89
	v_pk_add_f32 v[100:101], v[94:95], 1.0 op_sel_hi:[1,0]
	v_pk_fma_f32 v[102:103], v[94:95], s[8:9], v[92:93] op_sel_hi:[1,0,0]
	v_pk_fma_f32 v[100:101], v[96:97], v[100:101], v[100:101]
	v_pk_fma_f32 v[104:105], v[100:101], v[98:99], v[100:101]
	v_rcp_f32_e32 v104, v104
	v_rcp_f32_e32 v105, v105
	v_pk_fma_f32 v[102:103], v[102:103], v[98:99], v[102:103]
	v_pk_fma_f32 v[102:103], v[64:65], v[100:101], v[102:103]
	v_exp_f32_e32 v106, v87
	v_pk_mul_f32 v[64:65], v[102:103], v[104:105]
	v_exp_f32_e32 v108, v64
	v_exp_f32_e32 v109, v65
	v_exp_f32_e32 v107, v91
	v_pk_add_f32 v[110:111], v[108:109], 1.0 op_sel_hi:[1,0]
	v_pk_fma_f32 v[110:111], v[110:111], v[106:107], v[110:111]
	v_rcp_f32_e32 v110, v110
	v_rcp_f32_e32 v111, v111
	v_pk_add_f32 v[112:113], v[108:109], -1.0 op_sel_hi:[1,0]
	v_pk_mul_f32 v[112:113], v[112:113], v[110:111]
	v_cvt_pk_f16_f32 v114, v112, v113
	ds_write_b32 v81, v114 offset:6144
	s_waitcnt lgkmcnt(1)
	v_mfma_f32_16x16x32_f16 v[84:87], v[2:5], v[44:47], v[18:21]
	v_mfma_f32_16x16x32_f16 v[88:91], v[14:17], v[44:47], v[38:41]
	v_mfma_f32_16x16x32_f16 v[84:87], v[6:9], v[68:71], v[84:87]
	v_mfma_f32_16x16x32_f16 v[88:91], v[10:13], v[68:71], v[88:91]
	s_waitcnt lgkmcnt(0)
	s_barrier
	ds_read_b32 v125, v74 offset:128
	ds_read_b32 v126, v74 offset:192
	ds_read_b128 v[56:59], v75 offset:6144
	ds_read_b128 v[60:63], v75 offset:7168
	s_waitcnt lgkmcnt(2)
	v_add_f32_e32 v125, v125, v126
	v_mul_f32_e32 v126, 0x3fb8aa3b, v125
	v_exp_f32_e32 v126, v126
	v_cmp_lt_f32_e32 vcc, 0, v125
	v_mul_f32_e32 v125, 0x3f867d5f, v125
	v_fma_f32 v126, v126, v72, v73
	s_nop 0
	v_cndmask_b32_e32 v125, v126, v125, vcc
	s_mov_b64 s[16:17], exec
	s_mov_b64 exec, s[30:31]
	global_store_dword v124, v125, s[26:27] offset:8
	s_mov_b64 exec, s[16:17]
	s_waitcnt lgkmcnt(1)
	v_mfma_f32_16x16x32_f16 v[84:87], v[30:33], v[56:59], v[84:87]
	v_mfma_f32_16x16x32_f16 v[88:91], v[22:25], v[56:59], v[88:91]
	s_waitcnt lgkmcnt(0)
	v_mfma_f32_16x16x32_f16 v[84:87], v[34:37], v[60:63], v[84:87]
	v_mfma_f32_16x16x32_f16 v[88:91], v[26:29], v[60:63], v[88:91]
	ds_read_b128 v[44:47], v75 offset:2048
	ds_read_b128 v[68:71], v75 offset:3072
	s_nop 7
	v_exp_f32_e32 v94, v86
	v_exp_f32_e32 v95, v90
	v_exp_f32_e32 v96, v84
	v_exp_f32_e32 v97, v88
	v_exp_f32_e32 v98, v85
	v_exp_f32_e32 v99, v89
	v_pk_add_f32 v[100:101], v[94:95], 1.0 op_sel_hi:[1,0]
	v_pk_fma_f32 v[102:103], v[94:95], s[8:9], v[92:93] op_sel_hi:[1,0,0]
	v_pk_fma_f32 v[100:101], v[96:97], v[100:101], v[100:101]
	v_pk_fma_f32 v[104:105], v[100:101], v[98:99], v[100:101]
	v_rcp_f32_e32 v104, v104
	v_rcp_f32_e32 v105, v105
	v_pk_fma_f32 v[102:103], v[102:103], v[98:99], v[102:103]
	v_pk_fma_f32 v[102:103], v[64:65], v[100:101], v[102:103]
	v_exp_f32_e32 v106, v87
	v_pk_mul_f32 v[64:65], v[102:103], v[104:105]
	v_exp_f32_e32 v108, v64
	v_exp_f32_e32 v109, v65
	v_exp_f32_e32 v107, v91
	v_pk_add_f32 v[110:111], v[108:109], 1.0 op_sel_hi:[1,0]
	v_pk_fma_f32 v[110:111], v[110:111], v[106:107], v[110:111]
	v_rcp_f32_e32 v110, v110
	v_rcp_f32_e32 v111, v111
	v_pk_add_f32 v[112:113], v[108:109], -1.0 op_sel_hi:[1,0]
	v_pk_mul_f32 v[112:113], v[112:113], v[110:111]
	v_cvt_pk_f16_f32 v114, v112, v113
	ds_write_b32 v81, v114 offset:4096
	s_waitcnt lgkmcnt(1)
	v_mfma_f32_16x16x32_f16 v[84:87], v[2:5], v[44:47], v[18:21]
	v_mfma_f32_16x16x32_f16 v[88:91], v[14:17], v[44:47], v[38:41]
	v_mfma_f32_16x16x32_f16 v[84:87], v[6:9], v[68:71], v[84:87]
	v_mfma_f32_16x16x32_f16 v[88:91], v[10:13], v[68:71], v[88:91]
	s_waitcnt lgkmcnt(0)
	s_barrier
	ds_read_b32 v125, v74 offset:0
	ds_read_b32 v126, v74 offset:64
	ds_read_b128 v[56:59], v75 offset:4096
	ds_read_b128 v[60:63], v75 offset:5120
	s_waitcnt lgkmcnt(2)
	v_add_f32_e32 v125, v125, v126
	v_mul_f32_e32 v126, 0x3fb8aa3b, v125
	v_exp_f32_e32 v126, v126
	v_cmp_lt_f32_e32 vcc, 0, v125
	v_mul_f32_e32 v125, 0x3f867d5f, v125
	v_fma_f32 v126, v126, v72, v73
	s_nop 0
	v_cndmask_b32_e32 v125, v126, v125, vcc
	s_mov_b64 s[16:17], exec
	s_mov_b64 exec, s[30:31]
	global_store_dword v124, v125, s[26:27] offset:12
	s_mov_b64 exec, s[16:17]
	s_waitcnt lgkmcnt(1)
	v_mfma_f32_16x16x32_f16 v[84:87], v[30:33], v[56:59], v[84:87]
	v_mfma_f32_16x16x32_f16 v[88:91], v[22:25], v[56:59], v[88:91]
	s_waitcnt lgkmcnt(0)
	v_mfma_f32_16x16x32_f16 v[84:87], v[34:37], v[60:63], v[84:87]
	v_mfma_f32_16x16x32_f16 v[88:91], v[26:29], v[60:63], v[88:91]
	ds_read_b128 v[44:47], v75 offset:0
	ds_read_b128 v[68:71], v75 offset:1024
	s_nop 7
	v_exp_f32_e32 v94, v86
	v_exp_f32_e32 v95, v90
	v_exp_f32_e32 v96, v84
	v_exp_f32_e32 v97, v88
	v_exp_f32_e32 v98, v85
	v_exp_f32_e32 v99, v89
	v_pk_add_f32 v[100:101], v[94:95], 1.0 op_sel_hi:[1,0]
	v_pk_fma_f32 v[102:103], v[94:95], s[8:9], v[92:93] op_sel_hi:[1,0,0]
	v_pk_fma_f32 v[100:101], v[96:97], v[100:101], v[100:101]
	v_pk_fma_f32 v[104:105], v[100:101], v[98:99], v[100:101]
	v_rcp_f32_e32 v104, v104
	v_rcp_f32_e32 v105, v105
	v_pk_fma_f32 v[102:103], v[102:103], v[98:99], v[102:103]
	v_pk_fma_f32 v[102:103], v[64:65], v[100:101], v[102:103]
	v_exp_f32_e32 v106, v87
	v_pk_mul_f32 v[64:65], v[102:103], v[104:105]
	v_exp_f32_e32 v108, v64
	v_exp_f32_e32 v109, v65
	v_exp_f32_e32 v107, v91
	v_pk_add_f32 v[110:111], v[108:109], 1.0 op_sel_hi:[1,0]
	v_pk_fma_f32 v[110:111], v[110:111], v[106:107], v[110:111]
	v_rcp_f32_e32 v110, v110
	v_rcp_f32_e32 v111, v111
	v_pk_add_f32 v[112:113], v[108:109], -1.0 op_sel_hi:[1,0]
	v_pk_mul_f32 v[112:113], v[112:113], v[110:111]
	v_cvt_pk_f16_f32 v114, v112, v113
	ds_write_b32 v81, v114 offset:6144
	s_waitcnt lgkmcnt(1)
	v_mfma_f32_16x16x32_f16 v[84:87], v[2:5], v[44:47], v[18:21]
	v_mfma_f32_16x16x32_f16 v[88:91], v[14:17], v[44:47], v[38:41]
	v_mfma_f32_16x16x32_f16 v[84:87], v[6:9], v[68:71], v[84:87]
	v_mfma_f32_16x16x32_f16 v[88:91], v[10:13], v[68:71], v[88:91]
	s_waitcnt lgkmcnt(0)
	v_min_f32_e32 v64, 0x42700000, v64
	v_min_f32_e32 v65, 0x42700000, v65
	s_add_u32 s12, s12, 4
	v_add_u32_e32 v124, 16, v124
	s_cmp_lt_u32 s12, 452
	s_cbranch_scc1 .Lcb2_loop
	s_barrier
	ds_read_b32 v125, v74 offset:128
	ds_read_b32 v126, v74 offset:192
	ds_read_b128 v[56:59], v75 offset:6144
	ds_read_b128 v[60:63], v75 offset:7168
	s_waitcnt lgkmcnt(2)
	v_add_f32_e32 v125, v125, v126
	v_mul_f32_e32 v126, 0x3fb8aa3b, v125
	v_exp_f32_e32 v126, v126
	v_cmp_lt_f32_e32 vcc, 0, v125
	v_mul_f32_e32 v125, 0x3f867d5f, v125
	v_fma_f32 v126, v126, v72, v73
	s_nop 0
	v_cndmask_b32_e32 v125, v126, v125, vcc
	s_mov_b64 s[16:17], exec
	s_mov_b64 exec, s[30:31]
	global_store_dword v124, v125, s[26:27] offset:0
	s_mov_b64 exec, s[16:17]
	s_waitcnt lgkmcnt(0)
	s_waitcnt lgkmcnt(0)
	s_barrier
	ds_read_b32 v125, v74 offset:0
	ds_read_b32 v126, v74 offset:64
	s_waitcnt lgkmcnt(0)
	v_add_f32_e32 v125, v125, v126
	v_mul_f32_e32 v126, 0x3fb8aa3b, v125
	v_exp_f32_e32 v126, v126
	v_cmp_lt_f32_e32 vcc, 0, v125
	v_mul_f32_e32 v125, 0x3f867d5f, v125
	v_fma_f32 v126, v126, v72, v73
	s_nop 0
	v_cndmask_b32_e32 v125, v126, v125, vcc
	s_mov_b64 s[16:17], exec
	s_mov_b64 exec, s[30:31]
	global_store_dword v124, v125, s[26:27] offset:4
	s_mov_b64 exec, s[16:17]
	s_waitcnt lgkmcnt(0)
	s_endpgm
